# phase 10 modulated norm: gain/shift/scale loads of all 8 chunks issued before the row reduction (was one dependent load-compute-store round trip per chunk)
# speedup vs baseline: 1.0077x; 1.0026x over previous
; DI unsigned pk_bf16(float lo, float hi) { f32x2 v = {lo, hi}; hbf16x2 r = __builtin_convertvector(v, hbf16x2); return __builtin_bit_cast(unsigned, r); }
; DI void norm_mod_store(const f32x4 (&v)[8], const float* gain, const float* shift, const float* scale, bf16_t* hrow, int lane, unsigned char* h8row = nullptr) {
;     float ss = 0.f;
; #pragma unroll
;     for (int i = 0; i < 8; ++i) ss += v[i][0] * v[i][0] + v[i][1] * v[i][1] + v[i][2] * v[i][2] + v[i][3] * v[i][3];
;     ss = wave_sum(ss);
;     const float r = rsqrtf(ss * (1.0f / DM) + EPS);
; #pragma unroll
;     for (int i = 0; i < 8; ++i) {
;         const int col = 4 * lane + 256 * i;
;         const f32x4 g = *(const f32x4*)(gain + col), sh = *(const f32x4*)(shift + col), sc = *(const f32x4*)(scale + col);
;         const f32x4 h = (v[i] * r * g) * (1.0f + sc) + sh;
;         if (h8row) *(unsigned*)(h8row + col) = pk_fp8x4(h[0], h[1], h[2], h[3]);
;         else { u32x2 w; w.x = pk_bf16(h[0], h[1]); w.y = pk_bf16(h[2], h[3]); *(u32x2*)(hrow + col) = w; }
;     }
.LBB0_1123:
	s_or_b64 exec, exec, s[0:1]
	v_lshl_add_u64 v[76:77], v[78:79], 0, s[40:41]
	v_lshl_add_u64 v[78:79], v[78:79], 0, s[54:55]
	global_load_dwordx4 v[108:111], v[40:41], off
	v_lshl_add_u64 v[204:205], v[76:77], 0, v[38:39]
	v_lshl_add_u64 v[206:207], v[78:79], 0, v[38:39]
	global_load_dwordx4 v[140:143], v[204:205], off
	global_load_dwordx4 v[172:175], v[206:207], off
	global_load_dwordx4 v[112:115], v[40:41], off offset:1024
	v_lshl_add_u64 v[204:205], v[76:77], 0, v[62:63]
	v_lshl_add_u64 v[206:207], v[78:79], 0, v[62:63]
	global_load_dwordx4 v[144:147], v[204:205], off
	global_load_dwordx4 v[176:179], v[206:207], off
	global_load_dwordx4 v[116:119], v[40:41], off offset:2048
	v_lshl_add_u64 v[204:205], v[76:77], 0, v[64:65]
	v_lshl_add_u64 v[206:207], v[78:79], 0, v[64:65]
	global_load_dwordx4 v[148:151], v[204:205], off
	global_load_dwordx4 v[180:183], v[206:207], off
	global_load_dwordx4 v[120:123], v[40:41], off offset:3072
	v_lshl_add_u64 v[204:205], v[76:77], 0, v[66:67]
	v_lshl_add_u64 v[206:207], v[78:79], 0, v[66:67]
	global_load_dwordx4 v[152:155], v[204:205], off
	global_load_dwordx4 v[184:187], v[206:207], off
	global_load_dwordx4 v[124:127], v[42:43], off
	v_lshl_add_u64 v[204:205], v[76:77], 0, v[68:69]
	v_lshl_add_u64 v[206:207], v[78:79], 0, v[68:69]
	global_load_dwordx4 v[156:159], v[204:205], off
	global_load_dwordx4 v[188:191], v[206:207], off
	global_load_dwordx4 v[128:131], v[44:45], off
	v_lshl_add_u64 v[204:205], v[76:77], 0, v[70:71]
	v_lshl_add_u64 v[206:207], v[78:79], 0, v[70:71]
	global_load_dwordx4 v[160:163], v[204:205], off
	global_load_dwordx4 v[192:195], v[206:207], off
	global_load_dwordx4 v[132:135], v[46:47], off
	v_lshl_add_u64 v[204:205], v[76:77], 0, v[72:73]
	v_lshl_add_u64 v[206:207], v[78:79], 0, v[72:73]
	global_load_dwordx4 v[164:167], v[204:205], off
	global_load_dwordx4 v[196:199], v[206:207], off
	global_load_dwordx4 v[136:139], v[48:49], off
	v_lshl_add_u64 v[204:205], v[76:77], 0, v[74:75]
	v_lshl_add_u64 v[206:207], v[78:79], 0, v[74:75]
	global_load_dwordx4 v[168:171], v[204:205], off
	global_load_dwordx4 v[200:203], v[206:207], off
	v_mul_f32_e32 v80, v7, v7
	v_mul_f32_e32 v82, v3, v3
	v_fmac_f32_e32 v80, v6, v6
	v_fmac_f32_e32 v82, v2, v2
	v_fmac_f32_e32 v80, v8, v8
	v_fmac_f32_e32 v82, v4, v4
	v_fmac_f32_e32 v80, v9, v9
	v_fmac_f32_e32 v82, v5, v5
	v_add_f32_e32 v80, v80, v82
	v_mul_f32_e32 v82, v11, v11
	v_fmac_f32_e32 v82, v10, v10
	v_fmac_f32_e32 v82, v12, v12
	v_fmac_f32_e32 v82, v13, v13
	v_add_f32_e32 v80, v80, v82
	v_mul_f32_e32 v98, v31, v31
	v_fmac_f32_e32 v98, v30, v30
	v_fmac_f32_e32 v98, v32, v32
	v_fmac_f32_e32 v98, v33, v33
	v_mov_b32_e32 v100, v27
	v_mov_b32_e32 v101, v23
	v_add_f32_e32 v38, v80, v98
	v_mov_b32_e32 v98, v26
	v_mov_b32_e32 v99, v22
	v_pk_mul_f32 v[100:101], v[100:101], v[100:101]
	v_mov_b32_e32 v102, v28
	v_mov_b32_e32 v103, v24
	v_pk_fma_f32 v[98:99], v[98:99], v[98:99], v[100:101]
	v_mov_b32_e32 v104, v29
	v_mov_b32_e32 v105, v25
	v_pk_fma_f32 v[98:99], v[102:103], v[102:103], v[98:99]
	v_mov_b32_e32 v100, v19
	v_pk_fma_f32 v[98:99], v[104:105], v[104:105], v[98:99]
	v_mov_b32_e32 v101, v15
	v_add_f32_e32 v38, v38, v98
	v_add_f32_e32 v38, v38, v99
	v_mov_b32_e32 v98, v18
	v_mov_b32_e32 v99, v14
	v_pk_mul_f32 v[100:101], v[100:101], v[100:101]
	v_mov_b32_e32 v102, v20
	v_mov_b32_e32 v103, v16
	v_pk_fma_f32 v[98:99], v[98:99], v[98:99], v[100:101]
	v_mov_b32_e32 v104, v21
	v_mov_b32_e32 v105, v17
	v_pk_fma_f32 v[98:99], v[102:103], v[102:103], v[98:99]
	v_add_u32_e32 v34, s6, v34
	v_pk_fma_f32 v[98:99], v[104:105], v[104:105], v[98:99]
	v_lshl_add_u64 v[52:53], v[52:53], 0, s[8:9]
	v_add_f32_e32 v38, v38, v98
	v_add_f32_e32 v38, v38, v99
	ds_bpermute_b32 v80, v1, v38
	v_lshl_add_u64 v[218:219], s[50:51], 0, v[58:59]
	v_lshl_add_u64 v[56:57], v[56:57], 0, s[10:11]
	v_lshl_add_u64 v[58:59], v[58:59], 0, s[12:13]
	v_lshl_add_u64 v[60:61], v[60:61], 0, s[14:15]
	s_waitcnt lgkmcnt(0)
	v_add_f32_e32 v38, v38, v80
	ds_bpermute_b32 v80, v37, v38
	v_lshl_add_u64 v[54:55], v[54:55], 0, s[10:11]
	s_waitcnt lgkmcnt(0)
	v_add_f32_e32 v38, v38, v80
	ds_bpermute_b32 v80, v81, v38
	s_waitcnt lgkmcnt(0)
	v_add_f32_e32 v38, v38, v80
	ds_bpermute_b32 v80, v86, v38
	s_waitcnt lgkmcnt(0)
	v_add_f32_e32 v38, v38, v80
	ds_bpermute_b32 v80, v87, v38
	s_waitcnt lgkmcnt(0)
	v_add_f32_e32 v38, v38, v80
	ds_bpermute_b32 v80, v88, v38
	s_waitcnt lgkmcnt(0)
	v_add_f32_e32 v38, v38, v80
	v_fmamk_f32 v38, v38, 0x3a000000, v35
	v_mul_f32_e32 v80, 0x4b800000, v38
	v_cmp_gt_f32_e32 vcc, s59, v38
	s_nop 1
	v_cndmask_b32_e32 v38, v38, v80, vcc
	v_rsq_f32_e32 v38, v38
	s_nop 0
	v_mul_f32_e32 v100, 0x45800000, v38
	s_nop 0
	v_cndmask_b32_e32 v38, v38, v100, vcc
	v_add_co_u32_e32 v218, vcc, s67, v218
	s_nop 1
	v_addc_co_u32_e32 v219, vcc, 0, v219, vcc
	v_cmp_lt_i32_e32 vcc, s68, v34
	s_or_b64 s[16:17], vcc, s[16:17]
	v_pk_mul_f32 v[6:7], v[6:7], v[38:39] op_sel_hi:[1,0]
	v_pk_mul_f32 v[8:9], v[8:9], v[38:39] op_sel_hi:[1,0]
	s_waitcnt vmcnt(21)
; DI unsigned pk_bf16(float lo, float hi) { f32x2 v = {lo, hi}; hbf16x2 r = __builtin_convertvector(v, hbf16x2); return __builtin_bit_cast(unsigned, r); }
; DI void norm_mod_store(const f32x4 (&v)[8], const float* gain, const float* shift, const float* scale, bf16_t* hrow, int lane, unsigned char* h8row = nullptr) {
;     ...
;     for (int i = 0; i < 8; ++i) {
;         const int col = 4 * lane + 256 * i;
;         const f32x4 g = *(const f32x4*)(gain + col), sh = *(const f32x4*)(shift + col), sc = *(const f32x4*)(scale + col);
;         const f32x4 h = (v[i] * r * g) * (1.0f + sc) + sh;
;         if (h8row) *(unsigned*)(h8row + col) = pk_fp8x4(h[0], h[1], h[2], h[3]);
;         else { u32x2 w; w.x = pk_bf16(h[0], h[1]); w.y = pk_bf16(h[2], h[3]); *(u32x2*)(hrow + col) = w; }
	v_pk_mul_f32 v[6:7], v[108:109], v[6:7]
	v_pk_mul_f32 v[8:9], v[110:111], v[8:9]
	v_pk_add_f32 v[172:173], v[172:173], 1.0 op_sel_hi:[1,0]
	v_pk_add_f32 v[174:175], v[174:175], 1.0 op_sel_hi:[1,0]
	v_pk_fma_f32 v[6:7], v[172:173], v[6:7], v[140:141]
	v_pk_fma_f32 v[8:9], v[174:175], v[8:9], v[142:143]
	v_med3_f32 v6, v6, s66, v89
	v_med3_f32 v7, v7, s66, v89
	v_cvt_pk_fp8_f32 v208, v6, v7
	v_med3_f32 v8, v8, s66, v89
	v_med3_f32 v9, v9, s66, v89
	v_cvt_pk_fp8_f32 v208, v8, v9 op_sel:[0,0,1]
	global_store_dword v[218:219], v208, off
	v_pk_mul_f32 v[2:3], v[2:3], v[38:39] op_sel_hi:[1,0]
	v_pk_mul_f32 v[4:5], v[4:5], v[38:39] op_sel_hi:[1,0]
	s_waitcnt vmcnt(19)
	v_pk_mul_f32 v[2:3], v[112:113], v[2:3]
	v_pk_mul_f32 v[4:5], v[114:115], v[4:5]
	v_pk_add_f32 v[176:177], v[176:177], 1.0 op_sel_hi:[1,0]
	v_pk_add_f32 v[178:179], v[178:179], 1.0 op_sel_hi:[1,0]
	v_pk_fma_f32 v[2:3], v[176:177], v[2:3], v[144:145]
	v_pk_fma_f32 v[4:5], v[178:179], v[4:5], v[146:147]
	v_med3_f32 v2, v2, s66, v89
	v_med3_f32 v3, v3, s66, v89
	v_cvt_pk_fp8_f32 v209, v2, v3
	v_med3_f32 v4, v4, s66, v89
	v_med3_f32 v5, v5, s66, v89
	v_cvt_pk_fp8_f32 v209, v4, v5 op_sel:[0,0,1]
	global_store_dword v[218:219], v209, off offset:256
	v_pk_mul_f32 v[10:11], v[10:11], v[38:39] op_sel_hi:[1,0]
	v_pk_mul_f32 v[12:13], v[12:13], v[38:39] op_sel_hi:[1,0]
	s_waitcnt vmcnt(17)
	v_pk_mul_f32 v[10:11], v[116:117], v[10:11]
	v_pk_mul_f32 v[12:13], v[118:119], v[12:13]
	v_pk_add_f32 v[180:181], v[180:181], 1.0 op_sel_hi:[1,0]
	v_pk_add_f32 v[182:183], v[182:183], 1.0 op_sel_hi:[1,0]
	v_pk_fma_f32 v[10:11], v[180:181], v[10:11], v[148:149]
	v_pk_fma_f32 v[12:13], v[182:183], v[12:13], v[150:151]
	v_med3_f32 v10, v10, s66, v89
	v_med3_f32 v11, v11, s66, v89
	v_cvt_pk_fp8_f32 v210, v10, v11
	v_med3_f32 v12, v12, s66, v89
	v_med3_f32 v13, v13, s66, v89
	v_cvt_pk_fp8_f32 v210, v12, v13 op_sel:[0,0,1]
	global_store_dword v[218:219], v210, off offset:512
	v_pk_mul_f32 v[30:31], v[30:31], v[38:39] op_sel_hi:[1,0]
	v_pk_mul_f32 v[32:33], v[32:33], v[38:39] op_sel_hi:[1,0]
	s_waitcnt vmcnt(15)
	v_pk_mul_f32 v[30:31], v[120:121], v[30:31]
	v_pk_mul_f32 v[32:33], v[122:123], v[32:33]
	v_pk_add_f32 v[184:185], v[184:185], 1.0 op_sel_hi:[1,0]
	v_pk_add_f32 v[186:187], v[186:187], 1.0 op_sel_hi:[1,0]
	v_pk_fma_f32 v[30:31], v[184:185], v[30:31], v[152:153]
	v_pk_fma_f32 v[32:33], v[186:187], v[32:33], v[154:155]
	v_med3_f32 v30, v30, s66, v89
	v_med3_f32 v31, v31, s66, v89
	v_cvt_pk_fp8_f32 v211, v30, v31
	v_med3_f32 v32, v32, s66, v89
	v_med3_f32 v33, v33, s66, v89
	v_cvt_pk_fp8_f32 v211, v32, v33 op_sel:[0,0,1]
	global_store_dword v[218:219], v211, off offset:768
	v_pk_mul_f32 v[26:27], v[26:27], v[38:39] op_sel_hi:[1,0]
	v_pk_mul_f32 v[28:29], v[28:29], v[38:39] op_sel_hi:[1,0]
	s_waitcnt vmcnt(13)
	v_pk_mul_f32 v[26:27], v[124:125], v[26:27]
	v_pk_mul_f32 v[28:29], v[126:127], v[28:29]
	v_pk_add_f32 v[188:189], v[188:189], 1.0 op_sel_hi:[1,0]
	v_pk_add_f32 v[190:191], v[190:191], 1.0 op_sel_hi:[1,0]
	v_pk_fma_f32 v[26:27], v[188:189], v[26:27], v[156:157]
	v_pk_fma_f32 v[28:29], v[190:191], v[28:29], v[158:159]
	v_med3_f32 v26, v26, s66, v89
	v_med3_f32 v27, v27, s66, v89
	v_cvt_pk_fp8_f32 v212, v26, v27
	v_med3_f32 v28, v28, s66, v89
	v_med3_f32 v29, v29, s66, v89
	v_cvt_pk_fp8_f32 v212, v28, v29 op_sel:[0,0,1]
	global_store_dword v[218:219], v212, off offset:1024
	v_pk_mul_f32 v[22:23], v[22:23], v[38:39] op_sel_hi:[1,0]
	v_pk_mul_f32 v[24:25], v[24:25], v[38:39] op_sel_hi:[1,0]
	s_waitcnt vmcnt(11)
	v_pk_mul_f32 v[22:23], v[128:129], v[22:23]
	v_pk_mul_f32 v[24:25], v[130:131], v[24:25]
	v_pk_add_f32 v[192:193], v[192:193], 1.0 op_sel_hi:[1,0]
	v_pk_add_f32 v[194:195], v[194:195], 1.0 op_sel_hi:[1,0]
	v_pk_fma_f32 v[22:23], v[192:193], v[22:23], v[160:161]
	v_pk_fma_f32 v[24:25], v[194:195], v[24:25], v[162:163]
	v_med3_f32 v22, v22, s66, v89
	v_med3_f32 v23, v23, s66, v89
	v_cvt_pk_fp8_f32 v213, v22, v23
	v_med3_f32 v24, v24, s66, v89
	v_med3_f32 v25, v25, s66, v89
	v_cvt_pk_fp8_f32 v213, v24, v25 op_sel:[0,0,1]
	global_store_dword v[218:219], v213, off offset:1280
	v_pk_mul_f32 v[18:19], v[18:19], v[38:39] op_sel_hi:[1,0]
	v_pk_mul_f32 v[20:21], v[20:21], v[38:39] op_sel_hi:[1,0]
	s_waitcnt vmcnt(9)
	v_pk_mul_f32 v[18:19], v[132:133], v[18:19]
	v_pk_mul_f32 v[20:21], v[134:135], v[20:21]
	v_pk_add_f32 v[196:197], v[196:197], 1.0 op_sel_hi:[1,0]
	v_pk_add_f32 v[198:199], v[198:199], 1.0 op_sel_hi:[1,0]
	v_pk_fma_f32 v[18:19], v[196:197], v[18:19], v[164:165]
	v_pk_fma_f32 v[20:21], v[198:199], v[20:21], v[166:167]
	v_med3_f32 v18, v18, s66, v89
	v_med3_f32 v19, v19, s66, v89
	v_cvt_pk_fp8_f32 v214, v18, v19
	v_med3_f32 v20, v20, s66, v89
	v_med3_f32 v21, v21, s66, v89
	v_cvt_pk_fp8_f32 v214, v20, v21 op_sel:[0,0,1]
	global_store_dword v[218:219], v214, off offset:1536
	v_pk_mul_f32 v[14:15], v[14:15], v[38:39] op_sel_hi:[1,0]
	v_pk_mul_f32 v[16:17], v[16:17], v[38:39] op_sel_hi:[1,0]
	s_waitcnt vmcnt(7)
	v_pk_mul_f32 v[14:15], v[136:137], v[14:15]
	v_pk_mul_f32 v[16:17], v[138:139], v[16:17]
	v_pk_add_f32 v[200:201], v[200:201], 1.0 op_sel_hi:[1,0]
	v_pk_add_f32 v[202:203], v[202:203], 1.0 op_sel_hi:[1,0]
	v_pk_fma_f32 v[14:15], v[200:201], v[14:15], v[168:169]
	v_pk_fma_f32 v[16:17], v[202:203], v[16:17], v[170:171]
	v_med3_f32 v14, v14, s66, v89
	v_med3_f32 v15, v15, s66, v89
	v_cvt_pk_fp8_f32 v215, v14, v15
	v_med3_f32 v16, v16, s66, v89
	v_med3_f32 v17, v17, s66, v89
	v_cvt_pk_fp8_f32 v215, v16, v17 op_sel:[0,0,1]
	global_store_dword v[218:219], v215, off offset:1792
	s_andn2_b64 exec, exec, s[16:17]
	s_cbranch_execz .LBB0_1130
